# scan loop head: carry the source's stored flag in an SGPR so steady-state steps wait vmcnt(32) (DMA only) instead of vmcnt(0) (also the 32 output stores); on top of v133
# baseline (speedup 1.0000x reference)
; #define VM_WAIT() asm volatile("s_waitcnt vmcnt(0)" ::: "memory")
; __device__ __forceinline__ void p4_scan(Frame& F) {
;     ...
;     const int nt = F.wave, c = lane & 31, hh = lane >> 5;
;     bf16_t* OGb = WSP(bf16_t, WS_OGB) + (size_t)dir * ML * 1024;
;     f32x16 S[4];
; #pragma unroll
;     for (int kt = 0; kt < 4; ++kt)
; #pragma unroll
;         for (int i = 0; i < 16; ++i) S[kt][i] = 0.f;
;     bool stored = false;
; #pragma unroll 1
;     for (int n = 0; n < NCHUNK; ++n) {
;         if (stored) asm volatile("s_waitcnt vmcnt(32)" ::: "memory"); else VM_WAIT();
.LBB0_628:
	v_readlane_b32 s34, v253, 0
	s_mov_b64 s[28:29], -1
	s_cmpk_lt_u32 s34, 0x100
	v_lshl_add_u64 v[138:139], s[26:27], 0, v[140:141]
	s_cbranch_scc0 .LBB0_644
	s_lshl_b32 s26, s58, 25
	s_add_u32 s26, s86, s26
	s_addc_u32 s28, s87, 0
	v_readlane_b32 s34, v253, 7
	s_lshl_b32 s61, s31, 13
	s_and_b32 s59, s80, 15
	s_lshl_b32 s60, s34, 11
	s_addk_i32 s61, 0xff00
	s_lshl_b32 s29, s30, 8
	s_add_u32 s26, s26, s29
	s_addc_u32 s29, s28, 0
	s_lshl_b32 s28, s34, 6
	v_and_b32_e32 v2, 31, v0
	s_add_u32 s28, s26, s28
	v_lshrrev_b32_e32 v6, 3, v162
	s_addc_u32 s29, s29, 0
	v_lshlrev_b32_e32 v2, 1, v2
	v_mov_b32_e32 v3, 0
	v_and_b32_e32 v7, 4, v6
	v_lshl_add_u64 v[4:5], s[28:29], 0, v[2:3]
	v_mov_b32_e32 v142, v2
	s_mov_b32 s100, 0
	s_add_u32 s98, s28, 0x59000000
	s_addc_u32 s99, s29, 0
	s_mov_b64 s[28:29], 0x59000000
	v_bitop3_b32 v2, v6, 63, 4 bitop3:0x6c
	v_cndmask_b32_e64 v141, v2, v7, s[0:1]
	v_or_b32_e32 v2, 1, v7
	v_bitop3_b32 v4, v6, 62, 4 bitop3:0x6c
	v_cndmask_b32_e64 v144, v4, v2, s[0:1]
	v_or_b32_e32 v2, 2, v7
	v_bitop3_b32 v4, v6, 61, 4 bitop3:0x6c
	v_cndmask_b32_e64 v145, v4, v2, s[0:1]
	v_or_b32_e32 v2, 3, v6
	v_bitop3_b32 v4, v6, 63, 3 bitop3:0x36
	v_cndmask_b32_e64 v146, v4, v2, s[0:1]
	v_or_b32_e32 v2, 8, v7
	v_bitop3_b32 v4, v6, 55, 4 bitop3:0x6c
	v_cndmask_b32_e64 v147, v4, v2, s[0:1]
	v_or_b32_e32 v2, 9, v7
	v_bitop3_b32 v4, v6, 54, 4 bitop3:0x6c
	v_cndmask_b32_e64 v148, v4, v2, s[0:1]
	v_or_b32_e32 v2, 10, v7
	v_bitop3_b32 v4, v6, 53, 4 bitop3:0x6c
	v_cndmask_b32_e64 v149, v4, v2, s[0:1]
	v_or_b32_e32 v2, 11, v6
	v_bitop3_b32 v4, v6, 55, 3 bitop3:0x36
	v_cndmask_b32_e64 v150, v4, v2, s[0:1]
	v_or_b32_e32 v2, 16, v7
	v_bitop3_b32 v4, v6, 47, 4 bitop3:0x6c
	v_cndmask_b32_e64 v151, v4, v2, s[0:1]
	v_or_b32_e32 v2, 17, v7
	v_bitop3_b32 v4, v6, 46, 4 bitop3:0x6c
	v_cndmask_b32_e64 v152, v4, v2, s[0:1]
	v_or_b32_e32 v2, 18, v7
	v_bitop3_b32 v4, v6, 45, 4 bitop3:0x6c
	v_cndmask_b32_e64 v153, v4, v2, s[0:1]
	v_or_b32_e32 v2, 19, v6
	v_bitop3_b32 v4, v6, 47, 3 bitop3:0x36
	v_cndmask_b32_e64 v154, v4, v2, s[0:1]
	v_or_b32_e32 v2, 24, v7
	v_bitop3_b32 v4, v6, 39, 4 bitop3:0x6c
	v_cndmask_b32_e64 v155, v4, v2, s[0:1]
	v_or_b32_e32 v2, 25, v7
	v_bitop3_b32 v4, v6, 38, 4 bitop3:0x6c
	v_cndmask_b32_e64 v156, v4, v2, s[0:1]
	v_or_b32_e32 v2, 26, v7
	v_bitop3_b32 v4, v6, 37, 4 bitop3:0x6c
	v_cndmask_b32_e64 v157, v4, v2, s[0:1]
	v_or_b32_e32 v2, 27, v6
	v_bitop3_b32 v4, v6, 39, 3 bitop3:0x36
	v_cndmask_b32_e64 v158, v4, v2, s[0:1]
	v_or_b32_e32 v2, 32, v7
	v_bitop3_b32 v4, v6, 31, 4 bitop3:0x6c
	v_cndmask_b32_e64 v159, v4, v2, s[0:1]
	v_or_b32_e32 v2, 33, v7
	v_bitop3_b32 v4, v6, 30, 4 bitop3:0x6c
	v_cndmask_b32_e64 v160, v4, v2, s[0:1]
	v_or_b32_e32 v2, 34, v7
	v_bitop3_b32 v4, v6, 29, 4 bitop3:0x6c
	v_cndmask_b32_e64 v161, v4, v2, s[0:1]
	v_or_b32_e32 v2, 35, v6
	v_bitop3_b32 v4, v6, 63, 35 bitop3:0x36
	v_cndmask_b32_e64 v163, v4, v2, s[0:1]
	v_or_b32_e32 v2, 40, v7
	v_bitop3_b32 v4, v6, 23, 4 bitop3:0x6c
	v_cndmask_b32_e64 v164, v4, v2, s[0:1]
	v_or_b32_e32 v2, 41, v7
	v_bitop3_b32 v4, v6, 22, 4 bitop3:0x6c
	v_cndmask_b32_e64 v165, v4, v2, s[0:1]
	v_or_b32_e32 v2, 42, v7
	v_bitop3_b32 v4, v6, 21, 4 bitop3:0x6c
	v_cndmask_b32_e64 v166, v4, v2, s[0:1]
	v_or_b32_e32 v2, 43, v6
	v_bitop3_b32 v4, v6, 20, 4 bitop3:0x6c
	v_cndmask_b32_e64 v167, v4, v2, s[0:1]
	v_or_b32_e32 v2, 48, v7
	v_bitop3_b32 v4, v6, 15, 4 bitop3:0x6c
	v_cndmask_b32_e64 v168, v4, v2, s[0:1]
	v_or_b32_e32 v2, 49, v7
	v_bitop3_b32 v4, v6, 14, 4 bitop3:0x6c
	v_cndmask_b32_e64 v169, v4, v2, s[0:1]
	v_or_b32_e32 v2, 50, v7
	v_bitop3_b32 v4, v6, 13, 4 bitop3:0x6c
	v_cndmask_b32_e64 v170, v4, v2, s[0:1]
	v_or_b32_e32 v2, 51, v6
	v_bitop3_b32 v4, v6, 12, 4 bitop3:0x6c
	v_cndmask_b32_e64 v171, v4, v2, s[0:1]
	v_or_b32_e32 v2, 56, v7
	v_bitop3_b32 v4, v6, 7, 4 bitop3:0x6c
	v_cndmask_b32_e64 v172, v4, v2, s[0:1]
	v_or_b32_e32 v2, 57, v7
	v_bitop3_b32 v4, v6, 6, 4 bitop3:0x6c
	v_cndmask_b32_e64 v173, v4, v2, s[0:1]
	v_or_b32_e32 v2, 58, v7
	v_bitop3_b32 v4, v6, 5, 4 bitop3:0x6c
	s_mov_b32 s27, 0
	s_lshl_b32 s26, s34, 10
	v_cndmask_b32_e64 v174, v4, v2, s[0:1]
	v_or_b32_e32 v2, 59, v6
	v_bitop3_b32 v4, v6, 4, v6 bitop3:0xc
	v_lshlrev_b32_e32 v1, 5, v162
	s_lshl_b32 s28, s50, 10
	s_mov_b32 s29, s27
	s_lshl_b32 s30, s51, 10
	s_mov_b32 s31, s27
	s_lshl_b32 s34, s52, 10
	s_mov_b32 s35, s27
	s_lshl_b32 s36, s53, 10
	s_mov_b32 s37, s27
	s_lshl_b32 s38, s54, 10
	s_mov_b32 s39, s27
	s_lshl_b32 s40, s55, 10
	s_mov_b32 s41, s27
	s_lshl_b32 s42, s56, 10
	s_mov_b32 s43, s27
	s_lshl_b32 s44, s57, 10
	s_mov_b32 s45, s27
	s_or_b32 s46, s26, 0x12000
	s_mov_b32 s47, s27
	v_cndmask_b32_e64 v175, v4, v2, s[0:1]
	s_mov_b64 s[48:49], 0
	s_movk_i32 s62, 0x86
	v_mov_b32_e32 v176, 0x12400
	s_mov_b32 s64, s27
	v_mov_b32_e32 v2, v3
	v_mov_b32_e32 v4, v3
	v_mov_b32_e32 v5, v3
	v_mov_b32_e32 v6, v3
	v_mov_b32_e32 v7, v3
	v_mov_b32_e32 v8, v3
	v_mov_b32_e32 v9, v3
	v_mov_b32_e32 v10, v3
	v_mov_b32_e32 v11, v3
	v_mov_b32_e32 v12, v3
	v_mov_b32_e32 v13, v3
	v_mov_b32_e32 v14, v3
	v_mov_b32_e32 v15, v3
	v_mov_b32_e32 v16, v3
	v_mov_b32_e32 v17, v3
	v_mov_b32_e32 v18, v3
	v_mov_b32_e32 v19, v3
	v_mov_b32_e32 v20, v3
	v_mov_b32_e32 v21, v3
	v_mov_b32_e32 v22, v3
	v_mov_b32_e32 v23, v3
	v_mov_b32_e32 v24, v3
	v_mov_b32_e32 v25, v3
	v_mov_b32_e32 v26, v3
	v_mov_b32_e32 v27, v3
	v_mov_b32_e32 v28, v3
	v_mov_b32_e32 v29, v3
	v_mov_b32_e32 v30, v3
	v_mov_b32_e32 v31, v3
	v_mov_b32_e32 v32, v3
	v_mov_b32_e32 v33, v3
	v_mov_b32_e32 v34, v3
	v_mov_b32_e32 v35, v3
	v_mov_b32_e32 v36, v3
	v_mov_b32_e32 v37, v3
	v_mov_b32_e32 v38, v3
	v_mov_b32_e32 v39, v3
	v_mov_b32_e32 v40, v3
	v_mov_b32_e32 v41, v3
	v_mov_b32_e32 v42, v3
	v_mov_b32_e32 v43, v3
	v_mov_b32_e32 v44, v3
	v_mov_b32_e32 v45, v3
	v_mov_b32_e32 v46, v3
	v_mov_b32_e32 v47, v3
	v_mov_b32_e32 v48, v3
	v_mov_b32_e32 v49, v3
	v_mov_b32_e32 v50, v3
	v_mov_b32_e32 v51, v3
	v_mov_b32_e32 v52, v3
	v_mov_b32_e32 v53, v3
	v_mov_b32_e32 v54, v3
	v_mov_b32_e32 v55, v3
	v_mov_b32_e32 v56, v3
	v_mov_b32_e32 v57, v3
	v_mov_b32_e32 v58, v3
	v_mov_b32_e32 v59, v3
	v_mov_b32_e32 v60, v3
	v_mov_b32_e32 v61, v3
	v_mov_b32_e32 v62, v3
	v_mov_b32_e32 v63, v3
	v_mov_b32_e32 v64, v3
	v_mov_b32_e32 v65, v3
	s_branch .LBB0_631

; #define VM_WAIT() asm volatile("s_waitcnt vmcnt(0)" ::: "memory")
; #define ISSUE(n) do { const unsigned char* _ub = STEP_UNIT(n); LAS unsigned char* _lb = F.lds + ((n) & 1) * UNIT_DMA; _Pragma("unroll") for (int _p = 0; _p < 10; ++_p) \
;             if (_p * 8 + wv < UNIT_DMA / 1024) __builtin_amdgcn_global_load_lds((const unsigned*)(_ub + (_p * 8 + wv) * 1024 + lane * 16), (LAS unsigned*)(_lb + (_p * 8 + wv) * 1024), 16, 0, 0); } while (0)
; __device__ __forceinline__ void p4_scan(Frame& F) {
;     ...
;     for (int n = 0; n < NCHUNK; ++n) {
;         if (stored) asm volatile("s_waitcnt vmcnt(32)" ::: "memory"); else VM_WAIT();
;         __builtin_amdgcn_s_barrier(); asm volatile("" ::: "memory");
;         if (n + 1 < NCHUNK) ISSUE(n + 1);
.LBB0_631:
	s_andn2_b64 vcc, exec, s[48:49]
	s_mov_b64 s[48:49], -1
	s_cbranch_vccz .LBB0_633
	s_cmp_eq_u32 s100, 1
	s_cbranch_scc1 .Lscan_w32
	s_waitcnt vmcnt(0)
	s_branch .Lscan_wd
.Lscan_w32:
	s_waitcnt vmcnt(32)
.Lscan_wd:
	s_mov_b64 s[48:49], 0

; #define LAS __attribute__((address_space(3)))
; #define VM_WAIT() asm volatile("s_waitcnt vmcnt(0)" ::: "memory")
; #define ISSUE(n) do { const unsigned char* _ub = STEP_UNIT(n); LAS unsigned char* _lb = F.lds + ((n) & 1) * UNIT_DMA; _Pragma("unroll") for (int _p = 0; _p < 10; ++_p) \
;             if (_p * 8 + wv < UNIT_DMA / 1024) __builtin_amdgcn_global_load_lds((const unsigned*)(_ub + (_p * 8 + wv) * 1024 + lane * 16), (LAS unsigned*)(_lb + (_p * 8 + wv) * 1024), 16, 0, 0); } while (0)
; __device__ __forceinline__ void p4_scan(Frame& F) {
;     ...
;     for (int n = 0; n < NCHUNK; ++n) {
;         if (stored) asm volatile("s_waitcnt vmcnt(32)" ::: "memory"); else VM_WAIT();
;         __builtin_amdgcn_s_barrier(); asm volatile("" ::: "memory");
;         if (n + 1 < NCHUNK) ISSUE(n + 1);
;         const LAS unsigned char* lb = F.lds + (n & 1) * UNIT_DMA;
;         const float dlc = *(const LAS float*)(lb + UO_DL);
.LBB0_635:
	s_mov_b32 s100, 0
	s_barrier
	s_add_i32 s63, s64, 1
	s_cmp_eq_u32 s62, 3
	s_cbranch_scc1 .LBB0_641
	s_andn2_b64 vcc, exec, s[20:21]
	s_mov_b32 s48, s63
	s_cbranch_vccnz .LBB0_639
	s_cmp_gt_u32 s64, 2
	s_mov_b32 s48, s62
	s_cbranch_scc1 .LBB0_639
	s_sub_i32 s48, 2, s64

; #define LAS __attribute__((address_space(3)))
; __device__ __forceinline__ float bf_lo(unsigned w) { return __uint_as_float(w << 16); }
; __device__ __forceinline__ float bf_hi(unsigned w) { return __uint_as_float(w & 0xffff0000u); }
; #define MFMA32(a, b, c) __builtin_amdgcn_mfma_f32_32x32x16_bf16((a), (b), (c), 0, 0, 0)
; __device__ __forceinline__ bf16x8 pack_step(const f32x16& x, int s) { return __builtin_bit_cast(bf16x8, ((u32x4){pk(x[8 * s], x[8 * s + 1]), pk(x[8 * s + 2], x[8 * s + 3]), pk(x[8 * s + 4], x[8 * s + 5]), pk(x[8 * s + 6], x[8 * s + 7])})); }
; __device__ __forceinline__ void p4_scan(Frame& F) {
;     ...
;         const LAS unsigned char* lb = F.lds + (n & 1) * UNIT_DMA;
;         const float dlc = *(const LAS float*)(lb + UO_DL);
;         u32x4 ucur[2][2];
; #pragma unroll
;         for (int mt = 0; mt < 2; ++mt) { ucur[mt][0] = *(const LAS u32x4*)(lb + UO_U + (mt * 4 + nt) * 2048 + lane * 32); ucur[mt][1] = *(const LAS u32x4*)(lb + UO_U + (mt * 4 + nt) * 2048 + lane * 32 + 16); }
;     ...
;         f32x16 VN[2], O[2];
; #pragma unroll
;         for (int mt = 0; mt < 2; ++mt) {
; #pragma unroll
;             for (int p = 0; p < 4; ++p) { VN[mt][2 * p] = bf_lo(ucur[mt][0][p]); VN[mt][2 * p + 1] = bf_hi(ucur[mt][0][p]); VN[mt][8 + 2 * p] = bf_lo(ucur[mt][1][p]); VN[mt][8 + 2 * p + 1] = bf_hi(ucur[mt][1][p]); }
; #pragma unroll
;             for (int i = 0; i < 16; ++i) O[mt][i] = 0.f; }
; #pragma unroll
;         for (int kt = 0; kt < 4; ++kt) { const bf16x8 sb0 = pack_step(S[kt], 0), sb1 = pack_step(S[kt], 1);
; #pragma unroll
;             for (int mt = 0; mt < 2; ++mt) { const int fi = (mt * 4 + kt) * 2;
;                 VN[mt] = MFMA32(FRAG(UO_NW, fi), sb0, VN[mt]); VN[mt] = MFMA32(FRAG(UO_NW, fi + 1), sb1, VN[mt]);
;                 O[mt] = MFMA32(FRAG(UO_QD, fi), sb0, O[mt]); O[mt] = MFMA32(FRAG(UO_QD, fi + 1), sb1, O[mt]); } }
.LBB0_641:
	s_bitcmp1_b32 s64, 0
	s_cselect_b32 s48, 0x12400, 0
	s_add_i32 s48, s48, 0
	s_add_i32 s49, s48, s60
	v_add_u32_e32 v66, s49, v1
	v_add_u32_e32 v177, s48, v140
	ds_read_b128 v[70:73], v66 offset:57344
	v_add_u32_e32 v67, 0xe000, v66
	ds_read_b128 v[78:81], v66 offset:57360
	ds_read_b128 v[86:89], v67 offset:8192
	ds_read_b128 v[82:85], v67 offset:8208
	ds_read_b128 v[94:97], v177
	v_cvt_pk_bf16_f32 v90, v2, v3
	s_waitcnt lgkmcnt(0)
	v_lshlrev_b32_e32 v66, 16, v70
	v_and_b32_e32 v67, 0xffff0000, v70
	v_lshlrev_b32_e32 v74, 16, v78
	v_and_b32_e32 v75, 0xffff0000, v78
	v_lshlrev_b32_e32 v68, 16, v71
	v_and_b32_e32 v69, 0xffff0000, v71
	v_lshlrev_b32_e32 v76, 16, v79
	v_and_b32_e32 v77, 0xffff0000, v79
	v_lshlrev_b32_e32 v70, 16, v72
	v_and_b32_e32 v71, 0xffff0000, v72
	v_lshlrev_b32_e32 v78, 16, v80
	v_and_b32_e32 v79, 0xffff0000, v80
	v_lshlrev_b32_e32 v72, 16, v73
	v_and_b32_e32 v73, 0xffff0000, v73
	v_lshlrev_b32_e32 v80, 16, v81
	v_and_b32_e32 v81, 0xffff0000, v81
	v_cvt_pk_bf16_f32 v91, v4, v5
	v_cvt_pk_bf16_f32 v92, v6, v7
	v_cvt_pk_bf16_f32 v93, v8, v9
	ds_read_b128 v[98:101], v177 offset:1024
	ds_read_b128 v[130:133], v177 offset:56320
	v_mfma_f32_32x32x16_bf16 v[66:81], v[94:97], v[90:93], v[66:81]
	ds_read_b128 v[94:97], v177 offset:16384
	ds_read_b128 v[182:185], v177 offset:2048
	v_cvt_pk_bf16_f32 v178, v10, v11
	v_cvt_pk_bf16_f32 v179, v12, v13
	v_cvt_pk_bf16_f32 v180, v14, v15
	v_cvt_pk_bf16_f32 v181, v16, v17
	ds_read_b128 v[134:137], v177 offset:32768
	ds_read_b128 v[126:129], v177 offset:17408
	ds_read_b128 v[186:189], v177 offset:15360
	s_waitcnt lgkmcnt(0)
	v_mfma_f32_32x32x16_bf16 v[66:81], v[98:101], v[178:181], v[66:81]
	v_lshlrev_b32_e32 v114, 16, v86
	v_and_b32_e32 v115, 0xffff0000, v86
	v_lshlrev_b32_e32 v122, 16, v82
	v_and_b32_e32 v123, 0xffff0000, v82
	v_lshlrev_b32_e32 v116, 16, v87
	v_and_b32_e32 v117, 0xffff0000, v87
	v_lshlrev_b32_e32 v124, 16, v83
	v_mfma_f32_32x32x16_bf16 v[98:113], v[94:97], v[90:93], 0
	ds_read_b128 v[94:97], v177 offset:8192
	ds_read_b128 v[190:193], v177 offset:18432
	v_and_b32_e32 v125, 0xffff0000, v83
	v_lshlrev_b32_e32 v118, 16, v88
	v_and_b32_e32 v119, 0xffff0000, v88
	v_lshlrev_b32_e32 v120, 16, v89
	v_and_b32_e32 v121, 0xffff0000, v89
	ds_read_b128 v[194:197], v177 offset:7168
	v_mfma_f32_32x32x16_bf16 v[98:113], v[126:129], v[178:181], v[98:113]
	v_lshlrev_b32_e32 v126, 16, v84
	v_and_b32_e32 v127, 0xffff0000, v84
	v_lshlrev_b32_e32 v128, 16, v85
	v_and_b32_e32 v129, 0xffff0000, v85
	ds_read_b128 v[82:85], v177 offset:9216
	ds_read_b128 v[198:201], v177 offset:10240
	s_add_i32 s48, s48, 0x12000
	s_cmp_gt_u32 s64, 3
	s_waitcnt lgkmcnt(0)
	v_mfma_f32_32x32x16_bf16 v[114:129], v[94:97], v[90:93], v[114:129]
	v_mfma_f32_32x32x16_bf16 v[114:129], v[82:85], v[178:181], v[114:129]
	ds_read_b128 v[82:85], v177 offset:24576
	ds_read_b128 v[202:205], v177 offset:23552
	ds_read_b128 v[206:209], v177 offset:25600
	ds_read_b128 v[210:213], v177 offset:26624
	ds_read_b128 v[214:217], v177 offset:4096
	s_waitcnt lgkmcnt(0)
	v_mfma_f32_32x32x16_bf16 v[82:97], v[82:85], v[90:93], 0
	v_mfma_f32_32x32x16_bf16 v[82:97], v[206:209], v[178:181], v[82:97]
	v_cvt_pk_bf16_f32 v178, v18, v19
	v_cvt_pk_bf16_f32 v179, v20, v21
	v_cvt_pk_bf16_f32 v180, v22, v23
	v_cvt_pk_bf16_f32 v181, v24, v25
	v_cvt_pk_bf16_f32 v206, v26, v27
	v_cvt_pk_bf16_f32 v207, v28, v29
	v_cvt_pk_bf16_f32 v208, v30, v31
	v_mfma_f32_32x32x16_bf16 v[66:81], v[182:185], v[178:181], v[66:81]
	ds_read_b128 v[182:185], v177 offset:3072
	v_cvt_pk_bf16_f32 v209, v32, v33
	v_mfma_f32_32x32x16_bf16 v[98:113], v[190:193], v[178:181], v[98:113]
	s_waitcnt lgkmcnt(0)
	v_mfma_f32_32x32x16_bf16 v[66:81], v[182:185], v[206:209], v[66:81]
	ds_read_b128 v[182:185], v177 offset:19456
	ds_read_b128 v[190:193], v177 offset:20480
	v_mfma_f32_32x32x16_bf16 v[114:129], v[198:201], v[178:181], v[114:129]
	s_waitcnt lgkmcnt(0)
	v_mfma_f32_32x32x16_bf16 v[98:113], v[182:185], v[206:209], v[98:113]
	ds_read_b128 v[182:185], v177 offset:11264
	ds_read_b128 v[198:201], v177 offset:12288
	v_mfma_f32_32x32x16_bf16 v[82:97], v[210:213], v[178:181], v[82:97]
	v_cvt_pk_bf16_f32 v210, v42, v43
	v_cvt_pk_bf16_f32 v211, v44, v45
	v_cvt_pk_bf16_f32 v212, v46, v47
	v_cvt_pk_bf16_f32 v213, v48, v49
	s_waitcnt lgkmcnt(0)
	v_mfma_f32_32x32x16_bf16 v[114:129], v[182:185], v[206:209], v[114:129]
	ds_read_b128 v[178:181], v177 offset:27648
	ds_read_b128 v[182:185], v177 offset:28672
	s_waitcnt lgkmcnt(0)
	v_mfma_f32_32x32x16_bf16 v[82:97], v[178:181], v[206:209], v[82:97]
	v_cvt_pk_bf16_f32 v178, v34, v35
	v_cvt_pk_bf16_f32 v179, v36, v37
	v_cvt_pk_bf16_f32 v180, v38, v39
	v_cvt_pk_bf16_f32 v181, v40, v41
	ds_read_b128 v[206:209], v177 offset:5120
	s_nop 0
	v_mfma_f32_32x32x16_bf16 v[66:81], v[214:217], v[178:181], v[66:81]
	ds_read_b128 v[214:217], v177 offset:6144
	v_mfma_f32_32x32x16_bf16 v[98:113], v[190:193], v[178:181], v[98:113]
	s_waitcnt lgkmcnt(0)
	v_mfma_f32_32x32x16_bf16 v[66:81], v[206:209], v[210:213], v[66:81]
	ds_read_b128 v[190:193], v177 offset:21504
	ds_read_b128 v[206:209], v177 offset:22528
	v_mfma_f32_32x32x16_bf16 v[114:129], v[198:201], v[178:181], v[114:129]
	v_mfma_f32_32x32x16_bf16 v[82:97], v[182:185], v[178:181], v[82:97]
	s_waitcnt lgkmcnt(0)
	v_mfma_f32_32x32x16_bf16 v[98:113], v[190:193], v[210:213], v[98:113]
	ds_read_b128 v[190:193], v177 offset:13312
	ds_read_b128 v[198:201], v177 offset:14336
	ds_read_b128 v[178:181], v177 offset:29696
	ds_read_b128 v[182:185], v177 offset:30720
	s_waitcnt lgkmcnt(0)
; #define MFMA32(a, b, c) __builtin_amdgcn_mfma_f32_32x32x16_bf16((a), (b), (c), 0, 0, 0)
; __device__ __forceinline__ bf16x8 pack_step(const f32x16& x, int s) { return __builtin_bit_cast(bf16x8, ((u32x4){pk(x[8 * s], x[8 * s + 1]), pk(x[8 * s + 2], x[8 * s + 3]), pk(x[8 * s + 4], x[8 * s + 5]), pk(x[8 * s + 6], x[8 * s + 7])})); }
; __device__ __forceinline__ void p4_scan(Frame& F) {
;     ...
;         bf16x8 vb[2][2];
; #pragma unroll
;         for (int ct = 0; ct < 2; ++ct) { vb[ct][0] = pack_step(VN[ct], 0); vb[ct][1] = pack_step(VN[ct], 1); }
; #pragma unroll
;         for (int mt = 0; mt < 2; ++mt)
; #pragma unroll
;             for (int ct = 0; ct < 2; ++ct) { const int fi = (mt * 2 + ct) * 2; O[mt] = MFMA32(FRAG(UO_QK, fi), vb[ct][0], O[mt]); O[mt] = MFMA32(FRAG(UO_QK, fi + 1), vb[ct][1], O[mt]); }
; #pragma unroll
;         for (int kt = 0; kt < 4; ++kt) {
; #pragma unroll
;             for (int i = 0; i < 16; ++i) S[kt][i] *= dlc;
; #pragma unroll
;             for (int ct = 0; ct < 2; ++ct) { const int fi = (kt * 2 + ct) * 2; S[kt] = MFMA32(FRAG(UO_KDT, fi), vb[ct][0], S[kt]); S[kt] = MFMA32(FRAG(UO_KDT, fi + 1), vb[ct][1], S[kt]); } }
;     ...
;         const int cidx = STEP_CIDX(n);
;         stored = cidx >= CTXL / 64;
	v_mfma_f32_32x32x16_bf16 v[114:129], v[190:193], v[210:213], v[114:129]
	v_cvt_pk_bf16_f32 v190, v58, v59
	v_cvt_pk_bf16_f32 v191, v60, v61
	v_cvt_pk_bf16_f32 v192, v62, v63
	v_cvt_pk_bf16_f32 v193, v64, v65
	v_mfma_f32_32x32x16_bf16 v[82:97], v[178:181], v[210:213], v[82:97]
	v_cvt_pk_bf16_f32 v178, v50, v51
	v_cvt_pk_bf16_f32 v179, v52, v53
	v_cvt_pk_bf16_f32 v180, v54, v55
	v_cvt_pk_bf16_f32 v181, v56, v57
	s_nop 1
	v_mfma_f32_32x32x16_bf16 v[66:81], v[214:217], v[178:181], v[66:81]
	v_mfma_f32_32x32x16_bf16 v[98:113], v[206:209], v[178:181], v[98:113]
	v_mfma_f32_32x32x16_bf16 v[114:129], v[198:201], v[178:181], v[114:129]
	v_mfma_f32_32x32x16_bf16 v[82:97], v[182:185], v[178:181], v[82:97]
	ds_read_b128 v[178:181], v177 offset:31744
	v_mfma_f32_32x32x16_bf16 v[66:81], v[194:197], v[190:193], v[66:81]
	s_waitcnt lgkmcnt(0)
	v_mfma_f32_32x32x16_bf16 v[82:97], v[178:181], v[190:193], v[82:97]
	ds_read_b128 v[178:181], v177 offset:49152
	s_nop 8
	v_cvt_pk_bf16_f32 v66, v66, v67
	v_cvt_pk_bf16_f32 v67, v68, v69
	v_cvt_pk_bf16_f32 v68, v70, v71
	v_cvt_pk_bf16_f32 v69, v72, v73
	ds_read_b128 v[70:73], v177 offset:48128
	v_cvt_pk_bf16_f32 v74, v74, v75
	v_mfma_f32_32x32x16_bf16 v[98:113], v[202:205], v[190:193], v[98:113]
	v_cvt_pk_bf16_f32 v75, v76, v77
	v_cvt_pk_bf16_f32 v76, v78, v79
	v_cvt_pk_bf16_f32 v77, v80, v81
	ds_read_b128 v[78:81], v177 offset:51200
	s_waitcnt lgkmcnt(0)
	v_mfma_f32_32x32x16_bf16 v[98:113], v[178:181], v[66:69], v[98:113]
	ds_read_b128 v[178:181], v177 offset:50176
	v_mfma_f32_32x32x16_bf16 v[114:129], v[186:189], v[190:193], v[114:129]
	s_waitcnt lgkmcnt(0)
	v_mfma_f32_32x32x16_bf16 v[98:113], v[178:181], v[74:77], v[98:113]
	s_nop 9
	v_cvt_pk_bf16_f32 v114, v114, v115
	v_cvt_pk_bf16_f32 v115, v116, v117
	v_cvt_pk_bf16_f32 v116, v118, v119
	v_cvt_pk_bf16_f32 v117, v120, v121
	v_cvt_pk_bf16_f32 v118, v122, v123
	v_cvt_pk_bf16_f32 v119, v124, v125
	ds_read_b128 v[122:125], v177 offset:53248
	v_mfma_f32_32x32x16_bf16 v[98:113], v[78:81], v[114:117], v[98:113]
	ds_read_b128 v[78:81], v177 offset:52224
	v_cvt_pk_bf16_f32 v120, v126, v127
	v_cvt_pk_bf16_f32 v121, v128, v129
	s_waitcnt lgkmcnt(0)
	v_mfma_f32_32x32x16_bf16 v[82:97], v[122:125], v[66:69], v[82:97]
	v_mfma_f32_32x32x16_bf16 v[98:113], v[78:81], v[118:121], v[98:113]
	ds_read_b128 v[78:81], v177 offset:54272
	ds_read_b128 v[122:125], v177 offset:55296
	s_waitcnt lgkmcnt(0)
	v_mfma_f32_32x32x16_bf16 v[82:97], v[78:81], v[74:77], v[82:97]
	v_mov_b32_e32 v78, s48
	ds_read_b32 v126, v78
	s_cselect_b32 s48, 0x87, 3
	s_add_i32 s48, s48, s62
	s_add_i32 s65, s48, 0xffffff7a
	s_and_b64 s[48:49], s[0:1], exec
	s_waitcnt lgkmcnt(0)
	v_pk_mul_f32 v[16:17], v[16:17], v[126:127] op_sel_hi:[1,0]
	v_pk_mul_f32 v[14:15], v[14:15], v[126:127] op_sel_hi:[1,0]
	v_pk_mul_f32 v[12:13], v[12:13], v[126:127] op_sel_hi:[1,0]
	v_pk_mul_f32 v[10:11], v[10:11], v[126:127] op_sel_hi:[1,0]
	v_pk_mul_f32 v[8:9], v[8:9], v[126:127] op_sel_hi:[1,0]
	v_pk_mul_f32 v[6:7], v[6:7], v[126:127] op_sel_hi:[1,0]
	v_pk_mul_f32 v[4:5], v[4:5], v[126:127] op_sel_hi:[1,0]
	v_pk_mul_f32 v[2:3], v[2:3], v[126:127] op_sel_hi:[1,0]
	v_mfma_f32_32x32x16_bf16 v[82:97], v[122:125], v[114:117], v[82:97]
	ds_read_b128 v[78:81], v177 offset:33792
	ds_read_b128 v[122:125], v177 offset:34816
	v_mul_f32_e64 v32, v32, v126
	v_mul_f32_e64 v33, v33, v126
	v_mul_f32_e64 v30, v30, v126
	v_mul_f32_e64 v31, v31, v126
	v_pk_mul_f32 v[28:29], v[28:29], v[126:127] op_sel_hi:[1,0]
	v_pk_mul_f32 v[26:27], v[26:27], v[126:127] op_sel_hi:[1,0]
	v_pk_mul_f32 v[24:25], v[24:25], v[126:127] op_sel_hi:[1,0]
	v_pk_mul_f32 v[22:23], v[22:23], v[126:127] op_sel_hi:[1,0]
	v_mfma_f32_32x32x16_bf16 v[2:17], v[134:137], v[66:69], v[2:17]
	v_mul_f32_e64 v20, v20, v126
	v_mul_f32_e64 v21, v21, v126
	v_mul_f32_e64 v18, v18, v126
	v_mul_f32_e64 v19, v19, v126
	v_mul_f32_e64 v48, v48, v126
	v_mul_f32_e64 v49, v49, v126
	v_pk_mul_f32 v[46:47], v[46:47], v[126:127] op_sel_hi:[1,0]
	v_pk_mul_f32 v[44:45], v[44:45], v[126:127] op_sel_hi:[1,0]
	v_pk_mul_f32 v[42:43], v[42:43], v[126:127] op_sel_hi:[1,0]
	v_pk_mul_f32 v[40:41], v[40:41], v[126:127] op_sel_hi:[1,0]
	s_waitcnt lgkmcnt(0)
	v_mfma_f32_32x32x16_bf16 v[2:17], v[78:81], v[74:77], v[2:17]
	v_mul_f32_e64 v38, v38, v126
	v_mul_f32_e64 v39, v39, v126
	v_mul_f32_e64 v36, v36, v126
	v_mul_f32_e64 v37, v37, v126
	v_mul_f32_e64 v34, v34, v126
	v_mul_f32_e64 v35, v35, v126
	v_pk_mul_f32 v[64:65], v[64:65], v[126:127] op_sel_hi:[1,0]
	v_pk_mul_f32 v[62:63], v[62:63], v[126:127] op_sel_hi:[1,0]
	v_pk_mul_f32 v[60:61], v[60:61], v[126:127] op_sel_hi:[1,0]
	v_pk_mul_f32 v[58:59], v[58:59], v[126:127] op_sel_hi:[1,0]
	v_mfma_f32_32x32x16_bf16 v[2:17], v[122:125], v[114:117], v[2:17]
	ds_read_b128 v[78:81], v177 offset:35840
	ds_read_b128 v[122:125], v177 offset:36864
	v_mul_f32_e64 v56, v56, v126
	v_mul_f32_e64 v57, v57, v126
	v_mul_f32_e64 v54, v54, v126
	v_mul_f32_e64 v55, v55, v126
	v_pk_mul_f32 v[52:53], v[52:53], v[126:127] op_sel_hi:[1,0]
	v_pk_mul_f32 v[50:51], v[50:51], v[126:127] op_sel_hi:[1,0]
	s_cselect_b32 s64, s64, s65
	s_cmp_gt_i32 s64, 3
	s_waitcnt lgkmcnt(0)
	v_mfma_f32_32x32x16_bf16 v[18:33], v[122:125], v[66:69], v[18:33]
	s_cselect_b64 s[48:49], -1, 0
	s_cmp_lt_i32 s64, 4
	v_mfma_f32_32x32x16_bf16 v[2:17], v[78:81], v[118:121], v[2:17]
	ds_read_b128 v[78:81], v177 offset:37888
	ds_read_b128 v[122:125], v177 offset:38912
	s_waitcnt lgkmcnt(0)
	v_mfma_f32_32x32x16_bf16 v[18:33], v[78:81], v[74:77], v[18:33]
	v_mfma_f32_32x32x16_bf16 v[18:33], v[122:125], v[114:117], v[18:33]
	ds_read_b128 v[78:81], v177 offset:39936
	ds_read_b128 v[122:125], v177 offset:40960
	s_waitcnt lgkmcnt(0)
	v_mfma_f32_32x32x16_bf16 v[34:49], v[122:125], v[66:69], v[34:49]
	v_mfma_f32_32x32x16_bf16 v[18:33], v[78:81], v[118:121], v[18:33]
	ds_read_b128 v[78:81], v177 offset:41984
	ds_read_b128 v[122:125], v177 offset:43008
	s_waitcnt lgkmcnt(0)
	v_mfma_f32_32x32x16_bf16 v[34:49], v[78:81], v[74:77], v[34:49]
	v_mfma_f32_32x32x16_bf16 v[34:49], v[122:125], v[114:117], v[34:49]
	ds_read_b128 v[78:81], v177 offset:44032
	ds_read_b128 v[122:125], v177 offset:45056
	s_waitcnt lgkmcnt(0)
	v_mfma_f32_32x32x16_bf16 v[50:65], v[122:125], v[66:69], v[50:65]
	v_mfma_f32_32x32x16_bf16 v[34:49], v[78:81], v[118:121], v[34:49]
	ds_read_b128 v[66:69], v177 offset:46080
	ds_read_b128 v[78:81], v177 offset:47104
	s_waitcnt lgkmcnt(0)
	v_mfma_f32_32x32x16_bf16 v[50:65], v[66:69], v[74:77], v[50:65]
	v_mfma_f32_32x32x16_bf16 v[50:65], v[78:81], v[114:117], v[50:65]
	v_mfma_f32_32x32x16_bf16 v[82:97], v[130:133], v[118:121], v[82:97]
	v_mfma_f32_32x32x16_bf16 v[50:65], v[70:73], v[118:121], v[50:65]
	s_cbranch_scc1 .LBB0_630
; __device__ __forceinline__ bf16_t f2bf(float a) { return (bf16_t)(pk(a, 0.f) & 0xffffu); }
; __device__ __forceinline__ void p4_scan(Frame& F) {
;     ...
;         const int cidx = STEP_CIDX(n);
;         stored = cidx >= CTXL / 64;
;         if (cidx >= CTXL / 64) { const int rowbase = b * SEQ + (cidx - CTXL / 64) * 64;
; #pragma unroll
;             for (int mt = 0; mt < 2; ++mt)
; #pragma unroll
;                 for (int reg = 0; reg < 16; ++reg) { const int row = 32 * mt + (reg & 3) + 8 * (reg >> 2) + 4 * hh, prow = rowbase + (dir ? 63 - row : row);
;                     OGb[(size_t)prow * 1024 + h * 128 + 32 * nt + c] = f2bf(O[mt][reg]); } }
	s_mov_b32 s100, 1
	s_lshl_b32 s64, s64, 6
	s_add_i32 s64, s61, s64
	v_or_b32_e32 v66, s64, v141
	v_cvt_pk_bf16_f32 v68, v98, s0
	v_lshl_add_u32 v66, v66, 11, v142
	global_store_short v66, v68, s[98:99]
	v_or_b32_e32 v67, s64, v144
	v_cvt_pk_bf16_f32 v69, v99, s0
	v_lshl_add_u32 v67, v67, 11, v142
	global_store_short v67, v69, s[98:99]
	v_or_b32_e32 v66, s64, v145
	v_cvt_pk_bf16_f32 v68, v100, s0
	v_lshl_add_u32 v66, v66, 11, v142
	global_store_short v66, v68, s[98:99]
	v_or_b32_e32 v67, s64, v146
	v_cvt_pk_bf16_f32 v69, v101, s0
	v_lshl_add_u32 v67, v67, 11, v142
	global_store_short v67, v69, s[98:99]
	v_or_b32_e32 v66, s64, v147
	v_cvt_pk_bf16_f32 v68, v102, s0
	v_lshl_add_u32 v66, v66, 11, v142
	global_store_short v66, v68, s[98:99]
	v_or_b32_e32 v67, s64, v148
	v_cvt_pk_bf16_f32 v69, v103, s0
	v_lshl_add_u32 v67, v67, 11, v142
	global_store_short v67, v69, s[98:99]
	v_or_b32_e32 v66, s64, v149
	v_cvt_pk_bf16_f32 v68, v104, s0
	v_lshl_add_u32 v66, v66, 11, v142
	global_store_short v66, v68, s[98:99]
	v_or_b32_e32 v67, s64, v150
	v_cvt_pk_bf16_f32 v69, v105, s0
	v_lshl_add_u32 v67, v67, 11, v142
	global_store_short v67, v69, s[98:99]
	v_or_b32_e32 v66, s64, v151
	v_cvt_pk_bf16_f32 v68, v106, s0
	v_lshl_add_u32 v66, v66, 11, v142
	global_store_short v66, v68, s[98:99]
	v_or_b32_e32 v67, s64, v152
	v_cvt_pk_bf16_f32 v69, v107, s0
	v_lshl_add_u32 v67, v67, 11, v142
	global_store_short v67, v69, s[98:99]
	v_or_b32_e32 v66, s64, v153
	v_cvt_pk_bf16_f32 v68, v108, s0
	v_lshl_add_u32 v66, v66, 11, v142
	global_store_short v66, v68, s[98:99]
	v_or_b32_e32 v67, s64, v154
	v_cvt_pk_bf16_f32 v69, v109, s0
	v_lshl_add_u32 v67, v67, 11, v142
	global_store_short v67, v69, s[98:99]
	v_or_b32_e32 v66, s64, v155
	v_cvt_pk_bf16_f32 v68, v110, s0
	v_lshl_add_u32 v66, v66, 11, v142
	global_store_short v66, v68, s[98:99]
	v_or_b32_e32 v67, s64, v156
	v_cvt_pk_bf16_f32 v69, v111, s0
	v_lshl_add_u32 v67, v67, 11, v142
	global_store_short v67, v69, s[98:99]
	v_or_b32_e32 v66, s64, v157
	v_cvt_pk_bf16_f32 v68, v112, s0
	v_lshl_add_u32 v66, v66, 11, v142
	global_store_short v66, v68, s[98:99]
	v_or_b32_e32 v67, s64, v158
	v_cvt_pk_bf16_f32 v69, v113, s0
	v_lshl_add_u32 v67, v67, 11, v142
	global_store_short v67, v69, s[98:99]
	v_or_b32_e32 v66, s64, v159
	v_cvt_pk_bf16_f32 v68, v82, s0
	v_lshl_add_u32 v66, v66, 11, v142
	global_store_short v66, v68, s[98:99]
	v_or_b32_e32 v67, s64, v160
	v_cvt_pk_bf16_f32 v69, v83, s0
	v_lshl_add_u32 v67, v67, 11, v142
	global_store_short v67, v69, s[98:99]
	v_or_b32_e32 v66, s64, v161
	v_cvt_pk_bf16_f32 v68, v84, s0
	v_lshl_add_u32 v66, v66, 11, v142
	global_store_short v66, v68, s[98:99]
	v_or_b32_e32 v67, s64, v163
	v_cvt_pk_bf16_f32 v69, v85, s0
	v_lshl_add_u32 v67, v67, 11, v142
	global_store_short v67, v69, s[98:99]
	v_or_b32_e32 v66, s64, v164
	v_cvt_pk_bf16_f32 v68, v86, s0
	v_lshl_add_u32 v66, v66, 11, v142
	global_store_short v66, v68, s[98:99]
	v_or_b32_e32 v67, s64, v165
	v_cvt_pk_bf16_f32 v69, v87, s0
	v_lshl_add_u32 v67, v67, 11, v142
	global_store_short v67, v69, s[98:99]
	v_or_b32_e32 v66, s64, v166
	v_cvt_pk_bf16_f32 v68, v88, s0
	v_lshl_add_u32 v66, v66, 11, v142
	global_store_short v66, v68, s[98:99]
	v_or_b32_e32 v67, s64, v167
	v_cvt_pk_bf16_f32 v69, v89, s0
	v_lshl_add_u32 v67, v67, 11, v142
	global_store_short v67, v69, s[98:99]
	v_or_b32_e32 v66, s64, v168
	v_cvt_pk_bf16_f32 v68, v90, s0
	v_lshl_add_u32 v66, v66, 11, v142
	global_store_short v66, v68, s[98:99]
	v_or_b32_e32 v67, s64, v169
	v_cvt_pk_bf16_f32 v69, v91, s0
	v_lshl_add_u32 v67, v67, 11, v142
	global_store_short v67, v69, s[98:99]
	v_or_b32_e32 v66, s64, v170
	v_cvt_pk_bf16_f32 v68, v92, s0
	v_lshl_add_u32 v66, v66, 11, v142
	global_store_short v66, v68, s[98:99]
	v_or_b32_e32 v67, s64, v171
	v_cvt_pk_bf16_f32 v69, v93, s0
	v_lshl_add_u32 v67, v67, 11, v142
	global_store_short v67, v69, s[98:99]
	v_or_b32_e32 v66, s64, v172
	v_cvt_pk_bf16_f32 v68, v94, s0
	v_lshl_add_u32 v66, v66, 11, v142
	global_store_short v66, v68, s[98:99]
	v_or_b32_e32 v67, s64, v173
	v_cvt_pk_bf16_f32 v69, v95, s0
	v_lshl_add_u32 v67, v67, 11, v142
	global_store_short v67, v69, s[98:99]
	v_or_b32_e32 v66, s64, v174
	v_cvt_pk_bf16_f32 v68, v96, s0
	v_lshl_add_u32 v66, v66, 11, v142
	global_store_short v66, v68, s[98:99]
	v_or_b32_e32 v67, s64, v175
	v_cvt_pk_bf16_f32 v69, v97, s0
	v_lshl_add_u32 v67, v67, 11, v142
	global_store_short v67, v69, s[98:99]
	s_branch .LBB0_630
